# out-/down-projection K-loop: a unit's first two staging waits skip the previous unit's epilogue traffic (vmcnt 48)
# baseline (speedup 1.0000x reference)
; #define PG8_STAGE(bufoff, gbase, voff) do { _Pragma("unroll") for (int _i = 0; _i < 2; ++_i) \
;         __builtin_amdgcn_global_load_lds((const unsigned*)((const char*)(gbase) + (voff)[_i]), (PG8_LAS unsigned*)(lds + (bufoff) + ldsw + _i * 8192), 16, 0, 0); } while (0)
; #define PG8_WAIT_V(n) asm volatile("s_waitcnt vmcnt(" #n ")" ::: "memory")
; #define PG8_BAR __builtin_amdgcn_s_barrier()
; template <class Epi, class Sched, bool ALIGN_EPI = false, bool SP2 = false>
; __device__ __forceinline__ void gemm_phase(PG8_LAS unsigned char* lds, const Gemm g, const Sched& S, const Epi& E, const int tid) {
;     const int wid = __builtin_amdgcn_readfirstlane(tid >> 6), lane = tid & 63, wr = wid >> 2, wc = wid & 3, fr = lane & 15, fq = lane >> 4;
;     const int K = g.K, nt = K / BK;
;     unsigned voffA[2], voffB[2];
; #pragma unroll
;     for (int i = 0; i < 2; ++i) { int R, C; stage_rc(tid * 16 + i * 8192, R, C); const int Rb = Epi::PERM ? ((R & ~31) + perm32(R & 31)) : R;
;         voffA[i] = (unsigned)(R * g.lda + C) * 2u; voffB[i] = (unsigned)(Rb * K + C) * 2u; }
;     const size_t kstep = (size_t)(BK * 2);
;     const size_t hstep = (size_t)HALF * K * 2;
;     const size_t tstep = 2 * hstep;
;     const size_t hstepA = (size_t)HALF * g.lda * 2, tstepA = 2 * hstepA; const long padj = g.padj;
;     ...
;     const unsigned ldsw = (unsigned)wid * 1024u;
;     const int aoff = lds_byte(wr * 64 + fr, fq * 8), boff = lds_byte(wc * 32 + fr, fq * 8);
;     ...
;         PG8_WAIT_V(2); PG8_BAR;
;         PG8_STAGE(PG8_SB(1, 0), cB + kstep, voffB); PG8_STAGE(PG8_SA(1, 0), cA + kstep, voffA); PG8_STAGE(PG8_SB(1, 1), cB + hstep + kstep, voffB);
;         PG8_WAIT_V(6); PG8_BAR;
.LBB0_406:
	v_readlane_b32 s1, v254, 19
	v_mov_b32_e32 v199, v1
	v_mov_b32_e32 v203, v1
	s_cmp_lg_u32 s1, 12
	v_lshl_add_u64 v[8:9], s[26:27], 0, v[198:199]
	v_lshl_add_u64 v[12:13], s[8:9], 0, v[198:199]
	v_lshl_add_u64 v[14:15], s[8:9], 0, v[202:203]
	s_cselect_b64 s[8:9], -1, 0
	s_add_i32 s54, s47, 0x18000
	v_lshl_add_u64 v[10:11], s[26:27], 0, v[202:203]
	v_mov_b32_e32 v197, v1
	v_lshl_add_u64 v[8:9], v[8:9], 0, s[86:87]
	s_mov_b32 m0, s54
	s_add_i32 s55, s47, 0x1a000
	v_lshl_add_u64 v[16:17], s[28:29], 0, v[196:197]
	v_mov_b32_e32 v201, v1
	s_waitcnt vmcnt(2)
	s_barrier
	global_load_lds_dwordx4 v[8:9], off
	v_lshl_add_u64 v[8:9], v[10:11], 0, s[86:87]
	s_mov_b32 m0, s55
	s_add_i32 s56, s47, 0x8000
	v_lshl_add_u64 v[18:19], s[28:29], 0, v[200:201]
	global_load_lds_dwordx4 v[8:9], off
	v_lshl_add_u64 v[8:9], v[16:17], 0, s[86:87]
	s_mov_b32 m0, s56
	s_add_i32 s57, s47, 0xa000
	global_load_lds_dwordx4 v[8:9], off
	v_lshl_add_u64 v[8:9], v[18:19], 0, s[86:87]
	s_mov_b32 m0, s57
	s_add_i32 s58, s47, 0x1c000
	global_load_lds_dwordx4 v[8:9], off
	v_lshl_add_u64 v[8:9], v[12:13], 0, s[86:87]
	s_mov_b32 m0, s58
	s_add_i32 s59, s47, 0x1e000
	global_load_lds_dwordx4 v[8:9], off
	v_lshl_add_u64 v[8:9], v[14:15], 0, s[86:87]
	s_mov_b32 m0, s59
	v_bfe_u32 v7, v232, 4, 2
	global_load_lds_dwordx4 v[8:9], off
	v_and_b32_e32 v8, 15, v232
	v_lshlrev_b32_e32 v10, 4, v7
	v_lshl_or_b32 v195, s13, 6, v8
	v_lshl_or_b32 v8, v8, 6, v10
	v_lshlrev_b32_e32 v10, 2, v232
	s_and_b32 s60, s12, 3
	s_lshl_b32 s1, s13, 13
	v_and_b32_e32 v10, 32, v10
	v_bitop3_b32 v208, v8, s1, v10 bitop3:0xde
	s_lshl_b32 s1, s60, 12
	v_bitop3_b32 v209, s1, v8, v10 bitop3:0xf6
	v_and_b32_e32 v8, 64, v214
	v_lshlrev_b32_e32 v9, 3, v7
	v_cmp_eq_u32_e64 s[34:35], 0, v7
	v_xor_b32_e32 v7, 16, v214
	v_add_u32_e32 v8, 64, v8
	v_cmp_lt_i32_e32 vcc, v7, v8
	s_lshr_b32 s61, s11, 6
	s_cmpk_lt_u32 s10, 0x100
	v_cndmask_b32_e32 v7, v214, v7, vcc
	v_lshlrev_b32_e32 v211, 2, v7
	v_xor_b32_e32 v7, 32, v214
	v_cmp_lt_i32_e32 vcc, v7, v8
	v_readlane_b32 s1, v254, 12
	v_readlane_b32 s12, v254, 15
	v_cndmask_b32_e32 v7, v214, v7, vcc
	v_lshlrev_b32_e32 v212, 2, v7
	v_lshlrev_b32_e32 v7, 14, v4
	v_and_b32_e32 v7, 0xffff8000, v7
	v_lshl_add_u32 v5, v5, 11, v7
	v_and_b32_e32 v4, 1, v4
	v_lshl_or_b32 v4, v4, 6, v5
	s_cselect_b64 s[10:11], -1, 0
	s_ashr_i32 s63, s1, 31
	s_ashr_i32 s64, s12, 31
	v_lshl_add_u32 v204, v6, 1, v4
	v_lshlrev_b32_e32 v4, 14, v0
	v_readlane_b32 s13, v254, 16
	s_add_u32 s12, s74, 0x4000000
	v_and_b32_e32 v4, 0xffff8000, v4
	s_waitcnt vmcnt(6)
	s_addc_u32 s13, s75, 0
	v_lshl_add_u32 v2, v2, 11, v4
	v_and_b32_e32 v0, 1, v0
	s_add_u32 s14, s74, 0x3400000
	v_lshl_or_b32 v0, v0, 6, v2
	v_lshl_or_b32 v210, s60, 5, v9
	s_mov_b32 s62, 0
	s_addc_u32 s15, s75, 0
	v_mov_b32_e32 v205, v1
	v_lshl_add_u32 v206, v3, 1, v0
	v_mov_b32_e32 v207, v1
	s_barrier
	s_mov_b32 s100, 0
	s_branch .LBB0_409

; #define PG8_BAR __builtin_amdgcn_s_barrier()
; template <class Epi, class Sched, bool ALIGN_EPI = false, bool SP2 = false>
; __device__ __forceinline__ void gemm_phase(PG8_LAS unsigned char* lds, const Gemm g, const Sched& S, const Epi& E, const int tid) {
;     ...
;         const bool has_next = S.next(ui + 1, nxt);
;         const char* nA = has_next ? (const char*)g.A + (size_t)nxt.pm * tstepA : cA; const char* nB = has_next ? (const char*)g.Bt + (size_t)nxt.pn * tstep : cB;
;     ...
;         cur = nxt; cA = nA; cB = nB; ++ui;
;         if constexpr (ALIGN_EPI) { if (wr == 1) PG8_BAR; }
.LBB0_408:
	s_mov_b32 s100, 2
	s_andn2_b64 vcc, exec, s[0:1]
	s_mov_b32 s4, s16
	s_mov_b32 s0, s18
	s_mov_b64 s[26:27], s[22:23]
	s_mov_b64 s[28:29], s[20:21]
	s_cbranch_vccz .LBB0_492

; #define PG8_STAGE(bufoff, gbase, voff) do { _Pragma("unroll") for (int _i = 0; _i < 2; ++_i) \
;         __builtin_amdgcn_global_load_lds((const unsigned*)((const char*)(gbase) + (voff)[_i]), (PG8_LAS unsigned*)(lds + (bufoff) + ldsw + _i * 8192), 16, 0, 0); } while (0)
; #define PG8_LDA(dst, b, h) do { _Pragma("unroll") for (int m = 0; m < 4; ++m) _Pragma("unroll") for (int k = 0; k < 2; ++k) dst[m][k] = *(const PG8_LAS bf16x8*)(lds + PG8_SA(b, h) + aoff + m * 2048 + k * 1024); } while (0)
; #define PG8_LDB(dst, b, h) do { _Pragma("unroll") for (int n = 0; n < 2; ++n) _Pragma("unroll") for (int k = 0; k < 2; ++k) dst[n][k] = *(const PG8_LAS bf16x8*)(lds + PG8_SB(b, h) + boff + n * 2048 + k * 1024); } while (0)
; #define PG8_MMA(ai, bj, At, Bt) do { __builtin_amdgcn_s_setprio(1); _Pragma("unroll") for (int m = 0; m < 4; ++m) _Pragma("unroll") for (int n = 0; n < 2; ++n) _Pragma("unroll") for (int k = 0; k < 2; ++k) \
;         acc[ai][bj][m][n] = __builtin_amdgcn_mfma_f32_16x16x32_bf16(Bt[n][k], At[m][k], acc[ai][bj][m][n], 0, 0, 0); __builtin_amdgcn_s_setprio(0); } while (0)
; #define PG8_WAIT_V(n) asm volatile("s_waitcnt vmcnt(" #n ")" ::: "memory")
; #define PG8_WAIT_L(n) asm volatile("s_waitcnt lgkmcnt(" #n ")" ::: "memory")
; #define PG8_BAR __builtin_amdgcn_s_barrier()
; #define PG8_SCHED __builtin_amdgcn_sched_barrier(0)
; template <class Epi, class Sched, bool ALIGN_EPI = false, bool SP2 = false>
; __device__ __forceinline__ void gemm_phase(PG8_LAS unsigned char* lds, const Gemm g, const Sched& S, const Epi& E, const int tid) {
;     ...
;             const char* a1 = cA + PG8_KOFFA(t + 1);
;             const char* a2 = last ? nA : cA + PG8_KOFFA(t + 2); const char* b2 = last ? nB : cB + (size_t)(t + 2) * kstep;
;             const char* a3 = a2 + kstep; const char* b3 = b2 + kstep;
;             if (last && has_next) S.a_ready(nxt);
;             if constexpr (SP2) {
;             PG8_LDB(B0, 0, 0); PG8_LDB(B1, 0, 1); PG8_SCHED; PG8_LDA(At, 0, 0); PG8_STAGE(PG8_SA(1, 1), a1 + hstepA, voffA);
;             PG8_WAIT_V(8); PG8_WAIT_L(0); PG8_BAR; PG8_MMA(0, 0, At, B0); PG8_MMA(0, 1, At, B1); PG8_BAR; PG8_SCHED;
.LBB0_416:
	v_or_b32_e32 v0, 0x10000, v209
	v_add_u32_e32 v98, 0x10400, v209
	ds_read_b128 v[86:89], v0
	ds_read_b128 v[98:101], v98
	v_add_u32_e32 v0, 0x10800, v209
	v_add_u32_e32 v122, 0x10c00, v209
	ds_read_b128 v[106:109], v0
	ds_read_b128 v[122:125], v122
	v_or_b32_e32 v0, 0x14000, v209
	v_add_u32_e32 v142, 0x14400, v209
	s_lshr_b64 s[68:69], s[28:29], 4
	ds_read_b128 v[126:129], v0
	ds_read_b128 v[142:145], v142
	v_add_u32_e32 v0, 0x14800, v209
	v_add_u32_e32 v154, 0x14c00, v209
	v_mad_u64_u32 v[190:191], s[70:71], s68, v227, v[74:75]
	s_lshr_b32 s69, s29, 4
	ds_read_b128 v[150:153], v0
	ds_read_b128 v[154:157], v154
	s_mul_i32 s70, s69, 0x7ff800
	v_mad_u64_u32 v[222:223], s[68:69], s68, v227, v[76:77]
	s_add_u32 s68, s19, s30
	s_addc_u32 s69, s65, s31
	s_and_b64 s[40:41], exec, s[40:41]
	v_add_u32_e32 v191, s70, v191
	v_add_u32_e32 v223, s70, v223
	s_cselect_b32 s41, s1, s69
	s_cselect_b32 s40, s17, s68
	v_lshl_add_u64 v[222:223], v[222:223], 0, s[30:31]
	s_add_i32 m0, s47, 0xc000
	ds_read_b128 v[166:169], v208
	ds_read_b128 v[170:173], v208 offset:1024
	ds_read_b128 v[174:177], v208 offset:2048
	ds_read_b128 v[178:181], v208 offset:3072
	ds_read_b128 v[182:185], v208 offset:4096
	ds_read_b128 v[186:189], v208 offset:5120
	ds_read_b128 v[218:221], v208 offset:6144
	ds_read_b128 v[234:237], v208 offset:7168
	global_load_lds_dwordx4 v[222:223], off
	v_lshl_add_u64 v[190:191], v[190:191], 0, s[30:31]
	s_add_i32 m0, s47, 0xe000
	s_nop 0
	global_load_lds_dwordx4 v[190:191], off
	s_cmp_eq_u32 s100, 0
	s_cbranch_scc1 .Lrs_w8_0
	s_add_i32 s100, s100, -1
	s_waitcnt vmcnt(48)
	s_branch .Lrs_wd_0

; #define PG8_STAGE(bufoff, gbase, voff) do { _Pragma("unroll") for (int _i = 0; _i < 2; ++_i) \
;         __builtin_amdgcn_global_load_lds((const unsigned*)((const char*)(gbase) + (voff)[_i]), (PG8_LAS unsigned*)(lds + (bufoff) + ldsw + _i * 8192), 16, 0, 0); } while (0)
; #define PG8_LDA(dst, b, h) do { _Pragma("unroll") for (int m = 0; m < 4; ++m) _Pragma("unroll") for (int k = 0; k < 2; ++k) dst[m][k] = *(const PG8_LAS bf16x8*)(lds + PG8_SA(b, h) + aoff + m * 2048 + k * 1024); } while (0)
; #define PG8_MMA(ai, bj, At, Bt) do { __builtin_amdgcn_s_setprio(1); _Pragma("unroll") for (int m = 0; m < 4; ++m) _Pragma("unroll") for (int n = 0; n < 2; ++n) _Pragma("unroll") for (int k = 0; k < 2; ++k) \
;         acc[ai][bj][m][n] = __builtin_amdgcn_mfma_f32_16x16x32_bf16(Bt[n][k], At[m][k], acc[ai][bj][m][n], 0, 0, 0); __builtin_amdgcn_s_setprio(0); } while (0)
; #define PG8_WAIT_V(n) asm volatile("s_waitcnt vmcnt(" #n ")" ::: "memory")
; #define PG8_WAIT_L(n) asm volatile("s_waitcnt lgkmcnt(" #n ")" ::: "memory")
; #define PG8_BAR __builtin_amdgcn_s_barrier()
; #define PG8_SCHED __builtin_amdgcn_sched_barrier(0)
; template <class Epi, class Sched, bool ALIGN_EPI = false, bool SP2 = false>
; __device__ __forceinline__ void gemm_phase(PG8_LAS unsigned char* lds, const Gemm g, const Sched& S, const Epi& E, const int tid) {
;     ...
;             PG8_WAIT_V(8); PG8_WAIT_L(0); PG8_BAR; PG8_MMA(0, 0, At, B0); PG8_MMA(0, 1, At, B1); PG8_BAR; PG8_SCHED;
;             PG8_LDA(At, 0, 1); PG8_STAGE(PG8_SB(0, 0), b2, voffB); PG8_STAGE(PG8_SB(0, 1), b2 + hstep, voffB); PG8_STAGE(PG8_SA(0, 0), a2, voffA);
;             PG8_WAIT_V(8); PG8_WAIT_L(0); PG8_BAR; PG8_MMA(1, 0, At, B0); PG8_MMA(1, 1, At, B1); PG8_BAR; PG8_SCHED;
.Lrs_wd_0:
	s_waitcnt lgkmcnt(0)
	s_barrier
	s_setprio 1
	s_waitcnt lgkmcnt(0)
	v_mfma_f32_16x16x32_bf16 v[162:165], v[86:89], v[166:169], v[162:165]
	v_mfma_f32_16x16x32_bf16 v[158:161], v[106:109], v[166:169], v[158:161]
	v_mfma_f32_16x16x32_bf16 v[134:137], v[86:89], v[174:177], v[134:137]
	v_mfma_f32_16x16x32_bf16 v[130:133], v[106:109], v[174:177], v[130:133]
	v_mfma_f32_16x16x32_bf16 v[110:113], v[86:89], v[182:185], v[110:113]
	v_mfma_f32_16x16x32_bf16 v[102:105], v[106:109], v[182:185], v[102:105]
	v_mfma_f32_16x16x32_bf16 v[82:85], v[86:89], v[218:221], v[82:85]
	v_mfma_f32_16x16x32_bf16 v[78:81], v[106:109], v[218:221], v[78:81]
	v_mfma_f32_16x16x32_bf16 v[162:165], v[98:101], v[170:173], v[162:165]
	v_mfma_f32_16x16x32_bf16 v[158:161], v[122:125], v[170:173], v[158:161]
	v_mfma_f32_16x16x32_bf16 v[134:137], v[98:101], v[178:181], v[134:137]
	v_mfma_f32_16x16x32_bf16 v[130:133], v[122:125], v[178:181], v[130:133]
	v_mfma_f32_16x16x32_bf16 v[110:113], v[98:101], v[186:189], v[110:113]
	v_mfma_f32_16x16x32_bf16 v[102:105], v[122:125], v[186:189], v[102:105]
	v_mfma_f32_16x16x32_bf16 v[82:85], v[98:101], v[234:237], v[82:85]
	v_mfma_f32_16x16x32_bf16 v[78:81], v[122:125], v[234:237], v[78:81]
	s_setprio 0
	s_setprio 1
	v_mfma_f32_16x16x32_bf16 v[146:149], v[126:129], v[166:169], v[146:149]
	v_mfma_f32_16x16x32_bf16 v[138:141], v[150:153], v[166:169], v[138:141]
	v_mfma_f32_16x16x32_bf16 v[118:121], v[126:129], v[174:177], v[118:121]
	v_mfma_f32_16x16x32_bf16 v[114:117], v[150:153], v[174:177], v[114:117]
	v_mfma_f32_16x16x32_bf16 v[94:97], v[126:129], v[182:185], v[94:97]
	v_mfma_f32_16x16x32_bf16 v[90:93], v[150:153], v[182:185], v[90:93]
	v_mfma_f32_16x16x32_bf16 v[70:73], v[126:129], v[218:221], v[70:73]
	v_mfma_f32_16x16x32_bf16 v[66:69], v[150:153], v[218:221], v[66:69]
	v_mfma_f32_16x16x32_bf16 v[146:149], v[142:145], v[170:173], v[146:149]
	v_mfma_f32_16x16x32_bf16 v[138:141], v[154:157], v[170:173], v[138:141]
	v_mfma_f32_16x16x32_bf16 v[118:121], v[142:145], v[178:181], v[118:121]
	v_mfma_f32_16x16x32_bf16 v[114:117], v[154:157], v[178:181], v[114:117]
	v_mfma_f32_16x16x32_bf16 v[94:97], v[142:145], v[186:189], v[94:97]
	v_mfma_f32_16x16x32_bf16 v[90:93], v[154:157], v[186:189], v[90:93]
	v_mfma_f32_16x16x32_bf16 v[70:73], v[142:145], v[234:237], v[70:73]
	v_mfma_f32_16x16x32_bf16 v[66:69], v[154:157], v[234:237], v[66:69]
	s_setprio 0
	s_barrier
	s_mov_b32 m0, s5
	v_lshl_add_u64 v[190:191], s[40:41], 0, v[198:199]
	v_lshl_add_u64 v[222:223], s[40:41], 0, v[202:203]
	s_add_u32 s40, s40, s46
	ds_read_b128 v[166:169], v208 offset:16384
	ds_read_b128 v[170:173], v208 offset:17408
	ds_read_b128 v[174:177], v208 offset:18432
	ds_read_b128 v[178:181], v208 offset:19456
	ds_read_b128 v[182:185], v208 offset:20480
	ds_read_b128 v[186:189], v208 offset:21504
	ds_read_b128 v[218:221], v208 offset:22528
	ds_read_b128 v[234:237], v208 offset:23552
	global_load_lds_dwordx4 v[190:191], off
	s_mov_b32 m0, s48
	s_addc_u32 s41, s41, 0
	global_load_lds_dwordx4 v[222:223], off
	v_lshl_add_u64 v[228:229], s[40:41], 0, v[198:199]
	s_mov_b32 m0, s49
	v_lshl_add_u64 v[240:241], s[40:41], 0, v[202:203]
	global_load_lds_dwordx4 v[228:229], off
	s_mov_b32 m0, s50
	v_lshl_add_u64 v[242:243], s[38:39], 0, v[196:197]
	global_load_lds_dwordx4 v[240:241], off
	s_mov_b32 m0, s47
	v_lshl_add_u64 v[244:245], s[38:39], 0, v[200:201]
	global_load_lds_dwordx4 v[242:243], off
	s_mov_b32 m0, s51
	s_nop 0
	global_load_lds_dwordx4 v[244:245], off
	s_cmp_eq_u32 s100, 0
	s_cbranch_scc1 .Lrs_w8_1
	s_add_i32 s100, s100, -1
	s_waitcnt vmcnt(48)
	s_branch .Lrs_wd_1

; #define PG8_STAGE(bufoff, gbase, voff) do { _Pragma("unroll") for (int _i = 0; _i < 2; ++_i) \
;         __builtin_amdgcn_global_load_lds((const unsigned*)((const char*)(gbase) + (voff)[_i]), (PG8_LAS unsigned*)(lds + (bufoff) + ldsw + _i * 8192), 16, 0, 0); } while (0)
; #define PG8_LDA(dst, b, h) do { _Pragma("unroll") for (int m = 0; m < 4; ++m) _Pragma("unroll") for (int k = 0; k < 2; ++k) dst[m][k] = *(const PG8_LAS bf16x8*)(lds + PG8_SA(b, h) + aoff + m * 2048 + k * 1024); } while (0)
; #define PG8_LDB(dst, b, h) do { _Pragma("unroll") for (int n = 0; n < 2; ++n) _Pragma("unroll") for (int k = 0; k < 2; ++k) dst[n][k] = *(const PG8_LAS bf16x8*)(lds + PG8_SB(b, h) + boff + n * 2048 + k * 1024); } while (0)
; #define PG8_MMA(ai, bj, At, Bt) do { __builtin_amdgcn_s_setprio(1); _Pragma("unroll") for (int m = 0; m < 4; ++m) _Pragma("unroll") for (int n = 0; n < 2; ++n) _Pragma("unroll") for (int k = 0; k < 2; ++k) \
;         acc[ai][bj][m][n] = __builtin_amdgcn_mfma_f32_16x16x32_bf16(Bt[n][k], At[m][k], acc[ai][bj][m][n], 0, 0, 0); __builtin_amdgcn_s_setprio(0); } while (0)
; #define PG8_WAIT_V(n) asm volatile("s_waitcnt vmcnt(" #n ")" ::: "memory")
; #define PG8_WAIT_L(n) asm volatile("s_waitcnt lgkmcnt(" #n ")" ::: "memory")
; #define PG8_BAR __builtin_amdgcn_s_barrier()
; #define PG8_SCHED __builtin_amdgcn_sched_barrier(0)
; template <class Epi, class Sched, bool ALIGN_EPI = false, bool SP2 = false>
; __device__ __forceinline__ void gemm_phase(PG8_LAS unsigned char* lds, const Gemm g, const Sched& S, const Epi& E, const int tid) {
;     ...
;             PG8_WAIT_V(8); PG8_WAIT_L(0); PG8_BAR; PG8_MMA(1, 0, At, B0); PG8_MMA(1, 1, At, B1); PG8_BAR; PG8_SCHED;
;             PG8_LDB(B0, 1, 0); PG8_LDB(B1, 1, 1); PG8_SCHED; PG8_LDA(At, 1, 0); PG8_STAGE(PG8_SA(0, 1), a2 + hstepA, voffA);
;             PG8_WAIT_V(8); PG8_WAIT_L(0); PG8_BAR; PG8_MMA(0, 0, At, B0); PG8_MMA(0, 1, At, B1); PG8_BAR; PG8_SCHED;
.Lrs_wd_1:
	s_waitcnt lgkmcnt(0)
	s_barrier
	s_setprio 1
	s_waitcnt lgkmcnt(0)
	v_mfma_f32_16x16x32_bf16 v[62:65], v[86:89], v[166:169], v[62:65]
	v_mfma_f32_16x16x32_bf16 v[58:61], v[106:109], v[166:169], v[58:61]
	v_mfma_f32_16x16x32_bf16 v[46:49], v[86:89], v[174:177], v[46:49]
	v_mfma_f32_16x16x32_bf16 v[42:45], v[106:109], v[174:177], v[42:45]
	v_mfma_f32_16x16x32_bf16 v[30:33], v[86:89], v[182:185], v[30:33]
	v_mfma_f32_16x16x32_bf16 v[26:29], v[106:109], v[182:185], v[26:29]
	v_mfma_f32_16x16x32_bf16 v[14:17], v[86:89], v[218:221], v[14:17]
	v_mfma_f32_16x16x32_bf16 v[10:13], v[106:109], v[218:221], v[10:13]
	v_mfma_f32_16x16x32_bf16 v[62:65], v[98:101], v[170:173], v[62:65]
	v_mfma_f32_16x16x32_bf16 v[58:61], v[122:125], v[170:173], v[58:61]
	v_mfma_f32_16x16x32_bf16 v[46:49], v[98:101], v[178:181], v[46:49]
	v_mfma_f32_16x16x32_bf16 v[42:45], v[122:125], v[178:181], v[42:45]
	v_mfma_f32_16x16x32_bf16 v[30:33], v[98:101], v[186:189], v[30:33]
	v_mfma_f32_16x16x32_bf16 v[26:29], v[122:125], v[186:189], v[26:29]
	v_mfma_f32_16x16x32_bf16 v[14:17], v[98:101], v[234:237], v[14:17]
	v_mfma_f32_16x16x32_bf16 v[10:13], v[122:125], v[234:237], v[10:13]
	s_setprio 0
	s_setprio 1
	v_mfma_f32_16x16x32_bf16 v[54:57], v[126:129], v[166:169], v[54:57]
	v_mfma_f32_16x16x32_bf16 v[50:53], v[150:153], v[166:169], v[50:53]
	v_mfma_f32_16x16x32_bf16 v[38:41], v[126:129], v[174:177], v[38:41]
	v_mfma_f32_16x16x32_bf16 v[34:37], v[150:153], v[174:177], v[34:37]
	v_mfma_f32_16x16x32_bf16 v[22:25], v[126:129], v[182:185], v[22:25]
	v_mfma_f32_16x16x32_bf16 v[18:21], v[150:153], v[182:185], v[18:21]
	v_mfma_f32_16x16x32_bf16 v[6:9], v[126:129], v[218:221], v[6:9]
	v_mfma_f32_16x16x32_bf16 v[2:5], v[150:153], v[218:221], v[2:5]
	v_mfma_f32_16x16x32_bf16 v[54:57], v[142:145], v[170:173], v[54:57]
	v_mfma_f32_16x16x32_bf16 v[50:53], v[154:157], v[170:173], v[50:53]
	v_mfma_f32_16x16x32_bf16 v[38:41], v[142:145], v[178:181], v[38:41]
	v_mfma_f32_16x16x32_bf16 v[34:37], v[154:157], v[178:181], v[34:37]
	v_mfma_f32_16x16x32_bf16 v[22:25], v[142:145], v[186:189], v[22:25]
	v_mfma_f32_16x16x32_bf16 v[18:21], v[154:157], v[186:189], v[18:21]
	v_mfma_f32_16x16x32_bf16 v[6:9], v[142:145], v[234:237], v[6:9]
	v_mfma_f32_16x16x32_bf16 v[2:5], v[154:157], v[234:237], v[2:5]
	s_setprio 0
	s_barrier
	v_or_b32_e32 v0, 0x18000, v209
	v_add_u32_e32 v98, 0x18400, v209
	ds_read_b128 v[86:89], v0
	ds_read_b128 v[98:101], v98
	v_add_u32_e32 v0, 0x18800, v209
	v_add_u32_e32 v122, 0x18c00, v209
	ds_read_b128 v[106:109], v0
	ds_read_b128 v[122:125], v122
	v_or_b32_e32 v0, 0x1c000, v209
	v_add_u32_e32 v142, 0x1c400, v209
	ds_read_b128 v[126:129], v0
	ds_read_b128 v[142:145], v142
	v_add_u32_e32 v0, 0x1c800, v209
	v_add_u32_e32 v154, 0x1cc00, v209
	ds_read_b128 v[150:153], v0
	ds_read_b128 v[154:157], v154
	s_add_u32 s38, s38, 0x40000
	s_addc_u32 s39, s39, 0
	s_mov_b32 m0, s52
	v_lshl_add_u64 v[246:247], s[38:39], 0, v[196:197]
	ds_read_b128 v[166:169], v208 offset:32768
	ds_read_b128 v[170:173], v208 offset:33792
	ds_read_b128 v[174:177], v208 offset:34816
	ds_read_b128 v[178:181], v208 offset:35840
	ds_read_b128 v[182:185], v208 offset:36864
	ds_read_b128 v[186:189], v208 offset:37888
	ds_read_b128 v[218:221], v208 offset:38912
	ds_read_b128 v[234:237], v208 offset:39936
	global_load_lds_dwordx4 v[246:247], off
	v_lshl_add_u64 v[246:247], s[38:39], 0, v[200:201]
	s_mov_b32 m0, s53
	s_nop 0
	global_load_lds_dwordx4 v[246:247], off
	s_waitcnt vmcnt(8)
	s_waitcnt lgkmcnt(0)
	s_barrier
	s_setprio 1
	s_waitcnt lgkmcnt(0)
	v_mfma_f32_16x16x32_bf16 v[162:165], v[86:89], v[166:169], v[162:165]
	v_mfma_f32_16x16x32_bf16 v[158:161], v[106:109], v[166:169], v[158:161]
	v_mfma_f32_16x16x32_bf16 v[134:137], v[86:89], v[174:177], v[134:137]
	v_mfma_f32_16x16x32_bf16 v[130:133], v[106:109], v[174:177], v[130:133]
	v_mfma_f32_16x16x32_bf16 v[110:113], v[86:89], v[182:185], v[110:113]
	v_mfma_f32_16x16x32_bf16 v[102:105], v[106:109], v[182:185], v[102:105]
	v_mfma_f32_16x16x32_bf16 v[82:85], v[86:89], v[218:221], v[82:85]
	v_mfma_f32_16x16x32_bf16 v[78:81], v[106:109], v[218:221], v[78:81]
	v_mfma_f32_16x16x32_bf16 v[162:165], v[98:101], v[170:173], v[162:165]
	v_mfma_f32_16x16x32_bf16 v[158:161], v[122:125], v[170:173], v[158:161]
	v_mfma_f32_16x16x32_bf16 v[134:137], v[98:101], v[178:181], v[134:137]
	v_mfma_f32_16x16x32_bf16 v[130:133], v[122:125], v[178:181], v[130:133]
	v_mfma_f32_16x16x32_bf16 v[110:113], v[98:101], v[186:189], v[110:113]
	v_mfma_f32_16x16x32_bf16 v[102:105], v[122:125], v[186:189], v[102:105]
	v_mfma_f32_16x16x32_bf16 v[82:85], v[98:101], v[234:237], v[82:85]
	v_mfma_f32_16x16x32_bf16 v[78:81], v[122:125], v[234:237], v[78:81]
	s_setprio 0
	s_setprio 1
	v_mfma_f32_16x16x32_bf16 v[146:149], v[126:129], v[166:169], v[146:149]
	v_mfma_f32_16x16x32_bf16 v[138:141], v[150:153], v[166:169], v[138:141]
	v_mfma_f32_16x16x32_bf16 v[118:121], v[126:129], v[174:177], v[118:121]
	v_mfma_f32_16x16x32_bf16 v[114:117], v[150:153], v[174:177], v[114:117]
	v_mfma_f32_16x16x32_bf16 v[94:97], v[126:129], v[182:185], v[94:97]
	v_mfma_f32_16x16x32_bf16 v[90:93], v[150:153], v[182:185], v[90:93]
	v_mfma_f32_16x16x32_bf16 v[70:73], v[126:129], v[218:221], v[70:73]
	v_mfma_f32_16x16x32_bf16 v[66:69], v[150:153], v[218:221], v[66:69]
	v_mfma_f32_16x16x32_bf16 v[146:149], v[142:145], v[170:173], v[146:149]
	v_mfma_f32_16x16x32_bf16 v[138:141], v[154:157], v[170:173], v[138:141]
	v_mfma_f32_16x16x32_bf16 v[118:121], v[142:145], v[178:181], v[118:121]
	v_mfma_f32_16x16x32_bf16 v[114:117], v[154:157], v[178:181], v[114:117]
	v_mfma_f32_16x16x32_bf16 v[94:97], v[142:145], v[186:189], v[94:97]
	v_mfma_f32_16x16x32_bf16 v[90:93], v[154:157], v[186:189], v[90:93]
	v_mfma_f32_16x16x32_bf16 v[70:73], v[142:145], v[234:237], v[70:73]
	v_mfma_f32_16x16x32_bf16 v[66:69], v[154:157], v[234:237], v[66:69]
	s_setprio 0
	s_barrier
; #define PG8_STAGE(bufoff, gbase, voff) do { _Pragma("unroll") for (int _i = 0; _i < 2; ++_i) \
;         __builtin_amdgcn_global_load_lds((const unsigned*)((const char*)(gbase) + (voff)[_i]), (PG8_LAS unsigned*)(lds + (bufoff) + ldsw + _i * 8192), 16, 0, 0); } while (0)
; #define PG8_LDA(dst, b, h) do { _Pragma("unroll") for (int m = 0; m < 4; ++m) _Pragma("unroll") for (int k = 0; k < 2; ++k) dst[m][k] = *(const PG8_LAS bf16x8*)(lds + PG8_SA(b, h) + aoff + m * 2048 + k * 1024); } while (0)
; #define PG8_MMA(ai, bj, At, Bt) do { __builtin_amdgcn_s_setprio(1); _Pragma("unroll") for (int m = 0; m < 4; ++m) _Pragma("unroll") for (int n = 0; n < 2; ++n) _Pragma("unroll") for (int k = 0; k < 2; ++k) \
;         acc[ai][bj][m][n] = __builtin_amdgcn_mfma_f32_16x16x32_bf16(Bt[n][k], At[m][k], acc[ai][bj][m][n], 0, 0, 0); __builtin_amdgcn_s_setprio(0); } while (0)
; #define PG8_WAIT_V(n) asm volatile("s_waitcnt vmcnt(" #n ")" ::: "memory")
; #define PG8_WAIT_L(n) asm volatile("s_waitcnt lgkmcnt(" #n ")" ::: "memory")
; #define PG8_BAR __builtin_amdgcn_s_barrier()
; #define PG8_SCHED __builtin_amdgcn_sched_barrier(0)
; template <class Epi, class Sched, bool ALIGN_EPI = false, bool SP2 = false>
; __device__ __forceinline__ void gemm_phase(PG8_LAS unsigned char* lds, const Gemm g, const Sched& S, const Epi& E, const int tid) {
;     ...
;         for (int t = 0; t < nt; t += 2) {
;     ...
;             PG8_LDA(At, 1, 1); PG8_STAGE(PG8_SB(1, 0), b3, voffB); PG8_STAGE(PG8_SB(1, 1), b3 + hstep, voffB); PG8_STAGE(PG8_SA(1, 0), a3, voffA);
;             PG8_WAIT_V(8); PG8_WAIT_L(0); PG8_BAR; PG8_MMA(1, 0, At, B0); PG8_MMA(1, 1, At, B1); PG8_BAR; PG8_SCHED;
	s_mov_b32 m0, s54
	v_lshl_add_u64 v[190:191], v[190:191], 0, s[86:87]
	ds_read_b128 v[166:169], v208 offset:49152
	ds_read_b128 v[170:173], v208 offset:50176
	ds_read_b128 v[174:177], v208 offset:51200
	ds_read_b128 v[178:181], v208 offset:52224
	ds_read_b128 v[182:185], v208 offset:53248
	ds_read_b128 v[186:189], v208 offset:54272
	ds_read_b128 v[218:221], v208 offset:55296
	ds_read_b128 v[234:237], v208 offset:56320
	global_load_lds_dwordx4 v[190:191], off
	v_lshl_add_u64 v[190:191], v[222:223], 0, s[86:87]
	s_mov_b32 m0, s55
	s_nop 0
	global_load_lds_dwordx4 v[190:191], off
	v_lshl_add_u64 v[190:191], v[228:229], 0, s[86:87]
	s_mov_b32 m0, s58
	s_nop 0
	global_load_lds_dwordx4 v[190:191], off
	v_lshl_add_u64 v[190:191], v[240:241], 0, s[86:87]
	s_mov_b32 m0, s59
	s_nop 0
	global_load_lds_dwordx4 v[190:191], off
	v_lshl_add_u64 v[190:191], v[242:243], 0, s[86:87]
	s_mov_b32 m0, s56
	s_nop 0
	global_load_lds_dwordx4 v[190:191], off
	v_lshl_add_u64 v[190:191], v[244:245], 0, s[86:87]
	s_mov_b32 m0, s57
	s_nop 0
	global_load_lds_dwordx4 v[190:191], off
	s_waitcnt vmcnt(8)
	s_waitcnt lgkmcnt(0)
	s_barrier
	s_setprio 1
	s_waitcnt lgkmcnt(0)
	v_mfma_f32_16x16x32_bf16 v[62:65], v[86:89], v[166:169], v[62:65]
	v_mfma_f32_16x16x32_bf16 v[58:61], v[106:109], v[166:169], v[58:61]
	v_mfma_f32_16x16x32_bf16 v[46:49], v[86:89], v[174:177], v[46:49]
	v_mfma_f32_16x16x32_bf16 v[42:45], v[106:109], v[174:177], v[42:45]
	v_mfma_f32_16x16x32_bf16 v[30:33], v[86:89], v[182:185], v[30:33]
	v_mfma_f32_16x16x32_bf16 v[26:29], v[106:109], v[182:185], v[26:29]
	v_mfma_f32_16x16x32_bf16 v[14:17], v[86:89], v[218:221], v[14:17]
	v_mfma_f32_16x16x32_bf16 v[10:13], v[106:109], v[218:221], v[10:13]
	v_mfma_f32_16x16x32_bf16 v[62:65], v[98:101], v[170:173], v[62:65]
	v_mfma_f32_16x16x32_bf16 v[58:61], v[122:125], v[170:173], v[58:61]
	v_mfma_f32_16x16x32_bf16 v[46:49], v[98:101], v[178:181], v[46:49]
	v_mfma_f32_16x16x32_bf16 v[42:45], v[122:125], v[178:181], v[42:45]
	v_mfma_f32_16x16x32_bf16 v[30:33], v[98:101], v[186:189], v[30:33]
	v_mfma_f32_16x16x32_bf16 v[26:29], v[122:125], v[186:189], v[26:29]
	v_mfma_f32_16x16x32_bf16 v[14:17], v[98:101], v[234:237], v[14:17]
	v_mfma_f32_16x16x32_bf16 v[10:13], v[122:125], v[234:237], v[10:13]
	s_setprio 0
	s_setprio 1
	v_mfma_f32_16x16x32_bf16 v[54:57], v[126:129], v[166:169], v[54:57]
	v_mfma_f32_16x16x32_bf16 v[50:53], v[150:153], v[166:169], v[50:53]
	v_mfma_f32_16x16x32_bf16 v[38:41], v[126:129], v[174:177], v[38:41]
	v_mfma_f32_16x16x32_bf16 v[34:37], v[150:153], v[174:177], v[34:37]
	v_mfma_f32_16x16x32_bf16 v[22:25], v[126:129], v[182:185], v[22:25]
	v_mfma_f32_16x16x32_bf16 v[18:21], v[150:153], v[182:185], v[18:21]
	v_mfma_f32_16x16x32_bf16 v[6:9], v[126:129], v[218:221], v[6:9]
	v_mfma_f32_16x16x32_bf16 v[2:5], v[150:153], v[218:221], v[2:5]
	v_mfma_f32_16x16x32_bf16 v[54:57], v[142:145], v[170:173], v[54:57]
	v_mfma_f32_16x16x32_bf16 v[50:53], v[154:157], v[170:173], v[50:53]
	v_mfma_f32_16x16x32_bf16 v[38:41], v[142:145], v[178:181], v[38:41]
	v_mfma_f32_16x16x32_bf16 v[34:37], v[154:157], v[178:181], v[34:37]
	v_mfma_f32_16x16x32_bf16 v[22:25], v[142:145], v[186:189], v[22:25]
	v_mfma_f32_16x16x32_bf16 v[18:21], v[154:157], v[186:189], v[18:21]
	v_mfma_f32_16x16x32_bf16 v[6:9], v[142:145], v[234:237], v[6:9]
	v_mfma_f32_16x16x32_bf16 v[2:5], v[154:157], v[234:237], v[2:5]
	s_setprio 0
	s_barrier
	s_add_u32 s26, s26, 2
	s_addc_u32 s27, s27, 0
	s_add_i32 s38, s26, -2
	s_add_u32 s30, s30, 0x100
	s_addc_u32 s31, s31, 0
	s_add_u32 s28, s28, 2
	s_addc_u32 s29, s29, 0
	s_cmp_ge_u32 s38, s61
	s_cbranch_scc1 .LBB0_419
